# NSA softmax segment: rowmax via v_max3 chains, dead S-tile copies removed (on top of NSA prefetch/RMW + MoE order)
# speedup vs baseline: 1.0063x; 1.0063x over previous
; __device__ __forceinline__ float nsa_rowmax(const f32x16& p0, const f32x16& p1) { float mx = fmaxf(p0[0], p1[0]);
; #pragma unroll
;     for (int i = 1; i < 16; ++i) mx = fmaxf(mx, fmaxf(p0[i], p1[i]));
;     return mx; }
; __device__ __forceinline__ void nsa_unit(const Args& a, LAS unsigned char* lds, int b, int kvh, int qb) {
;     ...
;             float tmx = nsa_rowmax(p0, p1); tmx = lane_on ? tmx : NINF; tmx = fmaxf(tmx, __shfl_xor(tmx, 32));
;             float alpha = 1.f;
;             if (__any((tmx - mrun) * SM_C > 8.f)) { const float mnew = fmaxf(mrun, tmx); alpha = __builtin_amdgcn_exp2f((mrun - mnew) * SM_C); mrun = mnew;
; #pragma unroll
;                 for (int dt = 0; dt < 4; ++dt) o[dt] *= alpha; }
.LBB0_906:
	v_max3_f32 v34, v62, v63, v64
	v_max3_f32 v35, v78, v79, v80
	v_max3_f32 v34, v34, v65, v66
	v_max3_f32 v35, v35, v81, v82
	v_max3_f32 v34, v34, v67, v68
	v_max3_f32 v35, v35, v83, v84
	v_max3_f32 v34, v34, v69, v70
	v_max3_f32 v35, v35, v85, v86
	v_max3_f32 v34, v34, v71, v72
	v_max3_f32 v35, v35, v87, v88
	v_max3_f32 v34, v34, v73, v74
	v_max3_f32 v35, v35, v89, v90
	v_max3_f32 v34, v34, v75, v76
	v_max3_f32 v35, v35, v91, v92
	v_max3_f32 v34, v34, v77, v93
	v_max_f32_e32 v34, v34, v35
	v_cndmask_b32_e64 v34, v244, v34, s[2:3]
	ds_bpermute_b32 v35, v252, v34
	s_mov_b32 s4, 0x41000000
	s_waitcnt lgkmcnt(0)
	v_max_f32_e32 v35, v35, v35
	v_max_f32_e32 v46, v34, v35
	v_sub_f32_e32 v34, v46, v208
	v_mul_f32_e32 v34, 0x3e0293ee, v34
	v_cmp_lt_f32_e32 vcc, s4, v34
	s_cbranch_vccz .LBB0_910
	v_max_f32_e32 v34, v46, v46
	v_max_f32_e32 v35, v208, v208
	v_max_f32_e32 v34, v35, v34
	v_sub_f32_e32 v35, v208, v34
	v_mul_f32_e32 v35, 0x3e0293ee, v35
	v_exp_f32_e32 v46, v35
	v_mov_b32_e32 v208, v34
	v_pk_mul_f32 v[156:157], v[156:157], v[46:47] op_sel_hi:[1,0]
	v_pk_mul_f32 v[154:155], v[154:155], v[46:47] op_sel_hi:[1,0]
	v_pk_mul_f32 v[152:153], v[152:153], v[46:47] op_sel_hi:[1,0]
	v_pk_mul_f32 v[150:151], v[150:151], v[46:47] op_sel_hi:[1,0]
	v_pk_mul_f32 v[148:149], v[148:149], v[46:47] op_sel_hi:[1,0]
	v_pk_mul_f32 v[146:147], v[146:147], v[46:47] op_sel_hi:[1,0]
	v_pk_mul_f32 v[144:145], v[144:145], v[46:47] op_sel_hi:[1,0]
	v_pk_mul_f32 v[142:143], v[142:143], v[46:47] op_sel_hi:[1,0]
	v_pk_mul_f32 v[140:141], v[140:141], v[46:47] op_sel_hi:[1,0]
	v_pk_mul_f32 v[138:139], v[138:139], v[46:47] op_sel_hi:[1,0]
	v_pk_mul_f32 v[136:137], v[136:137], v[46:47] op_sel_hi:[1,0]
	v_pk_mul_f32 v[134:135], v[134:135], v[46:47] op_sel_hi:[1,0]
	v_pk_mul_f32 v[132:133], v[132:133], v[46:47] op_sel_hi:[1,0]
	v_pk_mul_f32 v[130:131], v[130:131], v[46:47] op_sel_hi:[1,0]
	v_pk_mul_f32 v[128:129], v[128:129], v[46:47] op_sel_hi:[1,0]
	v_pk_mul_f32 v[126:127], v[126:127], v[46:47] op_sel_hi:[1,0]
	v_pk_mul_f32 v[124:125], v[124:125], v[46:47] op_sel_hi:[1,0]
	v_pk_mul_f32 v[122:123], v[122:123], v[46:47] op_sel_hi:[1,0]
	v_pk_mul_f32 v[120:121], v[120:121], v[46:47] op_sel_hi:[1,0]
	v_pk_mul_f32 v[118:119], v[118:119], v[46:47] op_sel_hi:[1,0]
	v_pk_mul_f32 v[116:117], v[116:117], v[46:47] op_sel_hi:[1,0]
	v_pk_mul_f32 v[114:115], v[114:115], v[46:47] op_sel_hi:[1,0]
	v_pk_mul_f32 v[112:113], v[112:113], v[46:47] op_sel_hi:[1,0]
	v_pk_mul_f32 v[110:111], v[110:111], v[46:47] op_sel_hi:[1,0]
	v_pk_mul_f32 v[108:109], v[108:109], v[46:47] op_sel_hi:[1,0]
	v_pk_mul_f32 v[106:107], v[106:107], v[46:47] op_sel_hi:[1,0]
	v_pk_mul_f32 v[104:105], v[104:105], v[46:47] op_sel_hi:[1,0]
	v_pk_mul_f32 v[102:103], v[102:103], v[46:47] op_sel_hi:[1,0]
	v_pk_mul_f32 v[100:101], v[100:101], v[46:47] op_sel_hi:[1,0]
	v_pk_mul_f32 v[98:99], v[98:99], v[46:47] op_sel_hi:[1,0]
	v_pk_mul_f32 v[96:97], v[96:97], v[46:47] op_sel_hi:[1,0]
	v_pk_mul_f32 v[94:95], v[94:95], v[46:47] op_sel_hi:[1,0]
	s_branch .LBB0_911

; __device__ __forceinline__ bf16x8 nsa_pack8(const f32x16& p, int s) { u32x4 w; w.x = pg8::cvt_pk_bf16(p[8 * s + 0], p[8 * s + 1]); w.y = pg8::cvt_pk_bf16(p[8 * s + 2], p[8 * s + 3]); w.z = pg8::cvt_pk_bf16(p[8 * s + 4], p[8 * s + 5]); w.w = pg8::cvt_pk_bf16(p[8 * s + 6], p[8 * s + 7]); return __builtin_bit_cast(bf16x8, w); }
; __device__ __forceinline__ void nsa_unit(const Args& a, LAS unsigned char* lds, int b, int kvh, int qb) {
;     ...
;             const float nmc = lane_on ? -mrun * SM_C : NINF;
;             float ls = 0.f;
; #pragma unroll
;             for (int i = 0; i < 16; ++i) { p0[i] = __builtin_amdgcn_exp2f(fmaf(p0[i], SM_C, nmc)); p1[i] = __builtin_amdgcn_exp2f(fmaf(p1[i], SM_C, nmc)); ls += p0[i] + p1[i]; }
;             lrun = lrun * alpha + ls;
;             pf[0][0] = nsa_pack8(p0, 0); pf[0][1] = nsa_pack8(p0, 1); pf[1][0] = nsa_pack8(p1, 0); pf[1][1] = nsa_pack8(p1, 1);
.LBB0_911:
	v_mul_f32_e32 v34, 0xbe0293ee, v208
	v_cndmask_b32_e64 v190, v244, v34, s[2:3]
	v_fmamk_f32 v34, v78, 0x3e0293ee, v190
	v_exp_f32_e32 v78, v34
	v_fmamk_f32 v34, v62, 0x3e0293ee, v190
	v_exp_f32_e32 v62, v34
	v_fmamk_f32 v34, v79, 0x3e0293ee, v190
	v_fmamk_f32 v36, v80, 0x3e0293ee, v190
	v_exp_f32_e32 v79, v34
	v_fmamk_f32 v34, v63, 0x3e0293ee, v190
	v_exp_f32_e32 v80, v36
	v_fmamk_f32 v36, v64, 0x3e0293ee, v190
	v_exp_f32_e32 v63, v34
	v_exp_f32_e32 v64, v36
	v_fmamk_f32 v36, v81, 0x3e0293ee, v190
	v_exp_f32_e32 v81, v36
	v_fmamk_f32 v36, v65, 0x3e0293ee, v190
	v_exp_f32_e32 v65, v36
	v_add_f32_e32 v34, v78, v62
	v_add_f32_e32 v34, 0, v34
	v_add_f32_e32 v35, v79, v63
	v_add_f32_e32 v34, v35, v34
	v_add_f32_e32 v35, v80, v64
	v_add_f32_e32 v34, v35, v34
	v_add_f32_e32 v35, v81, v65
	v_add_f32_e32 v50, v35, v34
	v_fmamk_f32 v34, v82, 0x3e0293ee, v190
	v_exp_f32_e32 v35, v34
	v_fmamk_f32 v34, v66, 0x3e0293ee, v190
	v_exp_f32_e32 v37, v34
	v_fmamk_f32 v34, v83, 0x3e0293ee, v190
	v_fmamk_f32 v36, v67, 0x3e0293ee, v190
	v_fmamk_f32 v38, v84, 0x3e0293ee, v190
	v_exp_f32_e32 v34, v34
	v_exp_f32_e32 v36, v36
	v_exp_f32_e32 v39, v38
	v_fmamk_f32 v38, v68, 0x3e0293ee, v190
	v_exp_f32_e32 v41, v38
	v_fmamk_f32 v38, v85, 0x3e0293ee, v190
	v_fmamk_f32 v40, v69, 0x3e0293ee, v190
	v_exp_f32_e32 v38, v38
	v_exp_f32_e32 v40, v40
	v_pk_add_f32 v[48:49], v[34:35], v[36:37]
	v_fmamk_f32 v52, v88, 0x3e0293ee, v190
	v_add_f32_e32 v49, v49, v50
	v_add_f32_e32 v50, v48, v49
	v_pk_add_f32 v[48:49], v[38:39], v[40:41]
	v_exp_f32_e32 v53, v52
	v_add_f32_e32 v49, v49, v50
	v_add_f32_e32 v58, v48, v49
	v_fmamk_f32 v48, v86, 0x3e0293ee, v190
	v_exp_f32_e32 v49, v48
	v_fmamk_f32 v48, v70, 0x3e0293ee, v190
	v_exp_f32_e32 v51, v48
	v_fmamk_f32 v48, v87, 0x3e0293ee, v190
	v_fmamk_f32 v50, v71, 0x3e0293ee, v190
	v_exp_f32_e32 v48, v48
	v_exp_f32_e32 v50, v50
	v_fmamk_f32 v52, v72, 0x3e0293ee, v190
	v_exp_f32_e32 v55, v52
	v_fmamk_f32 v52, v89, 0x3e0293ee, v190
	v_fmamk_f32 v54, v73, 0x3e0293ee, v190
	v_exp_f32_e32 v52, v52
	v_exp_f32_e32 v54, v54
	v_pk_add_f32 v[56:57], v[48:49], v[50:51]
	v_fmamk_f32 v60, v92, 0x3e0293ee, v190
	v_add_f32_e32 v57, v57, v58
	v_add_f32_e32 v58, v56, v57
	v_pk_add_f32 v[56:57], v[52:53], v[54:55]
	v_exp_f32_e32 v61, v60
	v_add_f32_e32 v57, v57, v58
	v_add_f32_e32 v68, v56, v57
	v_fmamk_f32 v56, v90, 0x3e0293ee, v190
	v_exp_f32_e32 v57, v56
	v_fmamk_f32 v56, v74, 0x3e0293ee, v190
	v_exp_f32_e32 v59, v56
	v_fmamk_f32 v56, v91, 0x3e0293ee, v190
	v_fmamk_f32 v58, v75, 0x3e0293ee, v190
	v_exp_f32_e32 v56, v56
	v_exp_f32_e32 v58, v58
	v_fmamk_f32 v60, v76, 0x3e0293ee, v190
	v_exp_f32_e32 v211, v60
	v_fmamk_f32 v60, v93, 0x3e0293ee, v190
	v_fmac_f32_e32 v190, 0x3e0293ee, v77
	v_exp_f32_e32 v60, v60
	v_exp_f32_e32 v210, v190
	v_pk_add_f32 v[66:67], v[56:57], v[58:59]
	v_add_f32_e32 v67, v67, v68
	v_add_f32_e32 v66, v66, v67
	v_pk_add_f32 v[190:191], v[60:61], v[210:211]
	v_add_f32_e32 v191, v191, v66
	v_add_f32_e32 v212, v190, v191
	v_fmac_f32_e32 v212, v209, v46
	v_mov_b32_e32 v209, v212
	v_cvt_pk_bf16_f32 v190, v78, v79
	v_cvt_pk_bf16_f32 v191, v80, v81
	v_cvt_pk_bf16_f32 v192, v35, v34
	v_cvt_pk_bf16_f32 v193, v39, v38
	v_cvt_pk_bf16_f32 v194, v49, v48
	v_cvt_pk_bf16_f32 v195, v53, v52
	v_cvt_pk_bf16_f32 v196, v57, v56
	v_cvt_pk_bf16_f32 v197, v61, v60
	v_cvt_pk_bf16_f32 v198, v62, v63
	v_cvt_pk_bf16_f32 v199, v64, v65
	v_cvt_pk_bf16_f32 v200, v37, v36
	v_cvt_pk_bf16_f32 v201, v41, v40
	v_cvt_pk_bf16_f32 v202, v51, v50
	v_cvt_pk_bf16_f32 v203, v55, v54
	v_cvt_pk_bf16_f32 v204, v59, v58
	v_cvt_pk_bf16_f32 v205, v211, v210

; __device__ __forceinline__ float nsa_rowmax(const f32x16& p0, const f32x16& p1) { float mx = fmaxf(p0[0], p1[0]);
; #pragma unroll
;     for (int i = 1; i < 16; ++i) mx = fmaxf(mx, fmaxf(p0[i], p1[i]));
;     return mx; }
; __device__ __forceinline__ void nsa_unit(const Args& a, LAS unsigned char* lds, int b, int kvh, int qb) {
;     ...
;             float tmx = nsa_rowmax(p0, p1); tmx = lane_on ? tmx : NINF; tmx = fmaxf(tmx, __shfl_xor(tmx, 32));
;             float alpha = 1.f;
;             if (__any((tmx - mrun) * SM_C > 8.f)) { const float mnew = fmaxf(mrun, tmx); alpha = __builtin_amdgcn_exp2f((mrun - mnew) * SM_C); mrun = mnew;
; #pragma unroll
;                 for (int dt = 0; dt < 4; ++dt) o[dt] *= alpha; }
.LBB0_1852:
	v_max3_f32 v34, v62, v63, v64
	v_max3_f32 v35, v78, v79, v80
	v_max3_f32 v34, v34, v65, v66
	v_max3_f32 v35, v35, v81, v82
	v_max3_f32 v34, v34, v67, v68
	v_max3_f32 v35, v35, v83, v84
	v_max3_f32 v34, v34, v69, v70
	v_max3_f32 v35, v35, v85, v86
	v_max3_f32 v34, v34, v71, v72
	v_max3_f32 v35, v35, v87, v88
	v_max3_f32 v34, v34, v73, v74
	v_max3_f32 v35, v35, v89, v90
	v_max3_f32 v34, v34, v75, v76
	v_max3_f32 v35, v35, v91, v92
	v_max3_f32 v34, v34, v77, v93
	v_max_f32_e32 v34, v34, v35
	v_cndmask_b32_e64 v34, v244, v34, s[2:3]
	ds_bpermute_b32 v35, v252, v34
	s_mov_b32 s12, 0x41000000
	s_waitcnt lgkmcnt(0)
	v_max_f32_e32 v35, v35, v35
	v_max_f32_e32 v46, v34, v35
	v_sub_f32_e32 v34, v46, v208
	v_mul_f32_e32 v34, 0x3e0293ee, v34
	v_cmp_lt_f32_e32 vcc, s12, v34
	s_cbranch_vccz .LBB0_1856
	v_max_f32_e32 v34, v46, v46
	v_max_f32_e32 v35, v208, v208
	v_max_f32_e32 v34, v35, v34
	v_sub_f32_e32 v35, v208, v34
	v_mul_f32_e32 v35, 0x3e0293ee, v35
	v_exp_f32_e32 v46, v35
	v_mov_b32_e32 v208, v34
	v_pk_mul_f32 v[156:157], v[156:157], v[46:47] op_sel_hi:[1,0]
	v_pk_mul_f32 v[154:155], v[154:155], v[46:47] op_sel_hi:[1,0]
	v_pk_mul_f32 v[152:153], v[152:153], v[46:47] op_sel_hi:[1,0]
	v_pk_mul_f32 v[150:151], v[150:151], v[46:47] op_sel_hi:[1,0]
	v_pk_mul_f32 v[148:149], v[148:149], v[46:47] op_sel_hi:[1,0]
	v_pk_mul_f32 v[146:147], v[146:147], v[46:47] op_sel_hi:[1,0]
	v_pk_mul_f32 v[144:145], v[144:145], v[46:47] op_sel_hi:[1,0]
	v_pk_mul_f32 v[142:143], v[142:143], v[46:47] op_sel_hi:[1,0]
	v_pk_mul_f32 v[140:141], v[140:141], v[46:47] op_sel_hi:[1,0]
	v_pk_mul_f32 v[138:139], v[138:139], v[46:47] op_sel_hi:[1,0]
	v_pk_mul_f32 v[136:137], v[136:137], v[46:47] op_sel_hi:[1,0]
	v_pk_mul_f32 v[134:135], v[134:135], v[46:47] op_sel_hi:[1,0]
	v_pk_mul_f32 v[132:133], v[132:133], v[46:47] op_sel_hi:[1,0]
	v_pk_mul_f32 v[130:131], v[130:131], v[46:47] op_sel_hi:[1,0]
	v_pk_mul_f32 v[128:129], v[128:129], v[46:47] op_sel_hi:[1,0]
	v_pk_mul_f32 v[126:127], v[126:127], v[46:47] op_sel_hi:[1,0]
	v_pk_mul_f32 v[124:125], v[124:125], v[46:47] op_sel_hi:[1,0]
	v_pk_mul_f32 v[122:123], v[122:123], v[46:47] op_sel_hi:[1,0]
	v_pk_mul_f32 v[120:121], v[120:121], v[46:47] op_sel_hi:[1,0]
	v_pk_mul_f32 v[118:119], v[118:119], v[46:47] op_sel_hi:[1,0]
	v_pk_mul_f32 v[116:117], v[116:117], v[46:47] op_sel_hi:[1,0]
	v_pk_mul_f32 v[114:115], v[114:115], v[46:47] op_sel_hi:[1,0]
	v_pk_mul_f32 v[112:113], v[112:113], v[46:47] op_sel_hi:[1,0]
	v_pk_mul_f32 v[110:111], v[110:111], v[46:47] op_sel_hi:[1,0]
	v_pk_mul_f32 v[108:109], v[108:109], v[46:47] op_sel_hi:[1,0]
	v_pk_mul_f32 v[106:107], v[106:107], v[46:47] op_sel_hi:[1,0]
	v_pk_mul_f32 v[104:105], v[104:105], v[46:47] op_sel_hi:[1,0]
	v_pk_mul_f32 v[102:103], v[102:103], v[46:47] op_sel_hi:[1,0]
	v_pk_mul_f32 v[100:101], v[100:101], v[46:47] op_sel_hi:[1,0]
	v_pk_mul_f32 v[98:99], v[98:99], v[46:47] op_sel_hi:[1,0]
	v_pk_mul_f32 v[96:97], v[96:97], v[46:47] op_sel_hi:[1,0]
	v_pk_mul_f32 v[94:95], v[94:95], v[46:47] op_sel_hi:[1,0]
	s_branch .LBB0_1857
